# adaLN prologue GEMV with 16 weight loads in flight per trip (same fma order) on top of the max-free diff-attn path
# speedup vs baseline: 1.1193x; 1.0111x over previous
.LBB0_13:
	v_mov_b32_e32 v3, s16
	global_load_dword v16, v[6:7], off
	v_lshl_add_u64 v[6:7], v[6:7], 0, s[4:5]
	global_load_dword v17, v[6:7], off
	v_lshl_add_u64 v[6:7], v[6:7], 0, s[4:5]
	global_load_dword v18, v[6:7], off
	v_lshl_add_u64 v[6:7], v[6:7], 0, s[4:5]
	global_load_dword v19, v[6:7], off
	v_lshl_add_u64 v[6:7], v[6:7], 0, s[4:5]
	global_load_dword v20, v[6:7], off
	v_lshl_add_u64 v[6:7], v[6:7], 0, s[4:5]
	global_load_dword v21, v[6:7], off
	v_lshl_add_u64 v[6:7], v[6:7], 0, s[4:5]
	global_load_dword v22, v[6:7], off
	v_lshl_add_u64 v[6:7], v[6:7], 0, s[4:5]
	global_load_dword v23, v[6:7], off
	v_lshl_add_u64 v[6:7], v[6:7], 0, s[4:5]
	global_load_dword v24, v[6:7], off
	v_lshl_add_u64 v[6:7], v[6:7], 0, s[4:5]
	global_load_dword v25, v[6:7], off
	v_lshl_add_u64 v[6:7], v[6:7], 0, s[4:5]
	global_load_dword v26, v[6:7], off
	v_lshl_add_u64 v[6:7], v[6:7], 0, s[4:5]
	global_load_dword v27, v[6:7], off
	v_lshl_add_u64 v[6:7], v[6:7], 0, s[4:5]
	global_load_dword v28, v[6:7], off
	v_lshl_add_u64 v[6:7], v[6:7], 0, s[4:5]
	global_load_dword v29, v[6:7], off
	v_lshl_add_u64 v[6:7], v[6:7], 0, s[4:5]
	global_load_dword v30, v[6:7], off
	v_lshl_add_u64 v[6:7], v[6:7], 0, s[4:5]
	global_load_dword v31, v[6:7], off
	v_lshl_add_u64 v[6:7], v[6:7], 0, s[4:5]
	ds_read_b128 v[32:35], v3
	ds_read_b128 v[36:39], v3 offset:16
	ds_read_b128 v[40:43], v3 offset:32
	ds_read_b128 v[44:47], v3 offset:48
	ds_read_b128 v[48:51], v3 offset:4096
	ds_read_b128 v[52:55], v3 offset:4112
	ds_read_b128 v[56:59], v3 offset:4128
	ds_read_b128 v[60:63], v3 offset:4144
	ds_read_b128 v[64:67], v3 offset:8192
	ds_read_b128 v[68:71], v3 offset:8208
	ds_read_b128 v[72:75], v3 offset:8224
	ds_read_b128 v[76:79], v3 offset:8240
	s_add_i32 s8, s8, 16
	s_add_i32 s16, s16, 64
	s_waitcnt lgkmcnt(0)
	s_waitcnt vmcnt(15)
	v_fmac_f32_e32 v8, v16, v32
	v_fmac_f32_e32 v9, v16, v48
	v_fmac_f32_e32 v1, v16, v64
	s_waitcnt vmcnt(14)
	v_fmac_f32_e32 v8, v17, v33
	v_fmac_f32_e32 v9, v17, v49
	v_fmac_f32_e32 v1, v17, v65
	s_waitcnt vmcnt(13)
	v_fmac_f32_e32 v8, v18, v34
	v_fmac_f32_e32 v9, v18, v50
	v_fmac_f32_e32 v1, v18, v66
	s_waitcnt vmcnt(12)
	v_fmac_f32_e32 v8, v19, v35
	v_fmac_f32_e32 v9, v19, v51
	v_fmac_f32_e32 v1, v19, v67
	s_waitcnt vmcnt(11)
	v_fmac_f32_e32 v8, v20, v36
	v_fmac_f32_e32 v9, v20, v52
	v_fmac_f32_e32 v1, v20, v68
	s_waitcnt vmcnt(10)
	v_fmac_f32_e32 v8, v21, v37
	v_fmac_f32_e32 v9, v21, v53
	v_fmac_f32_e32 v1, v21, v69
	s_waitcnt vmcnt(9)
	v_fmac_f32_e32 v8, v22, v38
	v_fmac_f32_e32 v9, v22, v54
	v_fmac_f32_e32 v1, v22, v70
	s_waitcnt vmcnt(8)
	v_fmac_f32_e32 v8, v23, v39
	v_fmac_f32_e32 v9, v23, v55
	v_fmac_f32_e32 v1, v23, v71
	s_waitcnt vmcnt(7)
	v_fmac_f32_e32 v8, v24, v40
	v_fmac_f32_e32 v9, v24, v56
	v_fmac_f32_e32 v1, v24, v72
	s_waitcnt vmcnt(6)
	v_fmac_f32_e32 v8, v25, v41
	v_fmac_f32_e32 v9, v25, v57
	v_fmac_f32_e32 v1, v25, v73
	s_waitcnt vmcnt(5)
	v_fmac_f32_e32 v8, v26, v42
	v_fmac_f32_e32 v9, v26, v58
	v_fmac_f32_e32 v1, v26, v74
	s_waitcnt vmcnt(4)
	v_fmac_f32_e32 v8, v27, v43
	v_fmac_f32_e32 v9, v27, v59
	v_fmac_f32_e32 v1, v27, v75
	s_waitcnt vmcnt(3)
	v_fmac_f32_e32 v8, v28, v44
	v_fmac_f32_e32 v9, v28, v60
	v_fmac_f32_e32 v1, v28, v76
	s_waitcnt vmcnt(2)
	v_fmac_f32_e32 v8, v29, v45
	v_fmac_f32_e32 v9, v29, v61
	v_fmac_f32_e32 v1, v29, v77
	s_waitcnt vmcnt(1)
	v_fmac_f32_e32 v8, v30, v46
	v_fmac_f32_e32 v9, v30, v62
	v_fmac_f32_e32 v1, v30, v78
	s_waitcnt vmcnt(0)
	v_fmac_f32_e32 v8, v31, v47
	v_fmac_f32_e32 v9, v31, v63
	v_fmac_f32_e32 v1, v31, v79
	s_cmp_ge_u32 s8, s9
	s_cbranch_scc0 .LBB0_13
	v_readlane_b32 s4, v255, 6
	s_mulk_i32 s4, 0x300
	s_add_i32 s4, s4, 0
	s_cmpk_lt_u32 s3, 0xc0
	v_lshl_add_u32 v3, v2, 2, s4
	ds_write2st64_b32 v3, v8, v9 offset0:48 offset1:49
	ds_write_b32 v3, v1 offset:12800
	s_waitcnt lgkmcnt(0)
	s_barrier
	s_cbranch_scc0 .LBB0_16
	s_load_dwordx2 s[4:5], s[12:13], 0x28
	s_mulk_i32 s7, 0x1800
	v_add_u32_e32 v6, s7, v4
	v_ashrrev_i32_e32 v7, 31, v6
	s_waitcnt lgkmcnt(0)
	v_lshl_add_u64 v[6:7], v[6:7], 2, s[4:5]
	global_load_dword v1, v[6:7], off
	v_readlane_b32 s5, v255, 6
	s_add_i32 s4, s6, s5
	s_lshl_b32 s5, s5, 8
	s_add_i32 s5, s5, 0
	v_lshl_add_u32 v3, v2, 2, s5
	ds_read2st64_b32 v[6:7], v3 offset0:48 offset1:51
	ds_read2st64_b32 v[8:9], v3 offset0:54 offset1:57
	ds_read2st64_b32 v[10:11], v3 offset0:60 offset1:63
	ds_read2st64_b32 v[12:13], v3 offset0:66 offset1:69
	s_mul_hi_u32 s6, s4, 0x6000
	s_mulk_i32 s4, 0x6000
	s_add_u32 s4, s14, s4
	s_addc_u32 s5, s15, s6
	v_lshl_add_u64 v[4:5], v[4:5], 2, s[4:5]
	v_add_co_u32_e32 v4, vcc, 0x100000, v4
	s_waitcnt vmcnt(0) lgkmcnt(3)
	v_add_f32_e32 v1, v1, v6
	v_add_f32_e32 v1, v1, v7
	s_waitcnt lgkmcnt(2)
	v_add_f32_e32 v1, v1, v8
	v_add_f32_e32 v1, v1, v9
	s_waitcnt lgkmcnt(1)
	v_add_f32_e32 v1, v1, v10
	v_add_f32_e32 v1, v1, v11
	s_waitcnt lgkmcnt(0)
	v_add_f32_e32 v1, v1, v12
	v_add_f32_e32 v1, v1, v13
	v_addc_co_u32_e32 v5, vcc, 0, v5, vcc
	global_store_dword v[4:5], v1, off
